# speedup vs baseline: 1.0172x; 1.0172x over previous
_Z12oproj_kernelPKDF16_S0_PKfPf:
	s_load_dwordx8 s[4:11], s[0:1], 0x0
	s_lshl_b32 s0, s2, 2
	s_lshr_b32 s1, s2, 6
	s_and_b32 s0, s0, 28
	s_add_i32 s0, s0, s1
	v_bfe_u32 v14, v0, 6, 1
	s_bfe_u32 s13, s2, 0x30003
	s_lshl_b32 s12, s0, 7
	s_mul_i32 s0, s0, 0x44000
	v_bfe_u32 v12, v0, 4, 2
	v_and_b32_e32 v1, 7, v0
	v_lshlrev_b32_e32 v2, 2, v14
	s_mul_hi_i32 s1, s12, 0x880
	s_waitcnt lgkmcnt(0)
	s_add_u32 s0, s4, s0
	v_lshrrev_b32_e32 v13, 6, v0
	v_bitop3_b32 v1, v2, v1, v12 bitop3:0x36
	v_bfe_u32 v2, v0, 3, 3
	s_addc_u32 s1, s5, s1
	s_mul_i32 s2, s13, 0x44000
	v_lshl_or_b32 v2, v13, 3, v2
	s_add_u32 s2, s6, s2
	v_mul_u32_u24_e32 v2, 0x440, v2
	s_addc_u32 s3, s7, 0
	v_lshlrev_b32_e32 v2, 1, v2
	v_mov_b32_e32 v3, 0
	v_lshl_add_u64 v[4:5], s[0:1], 0, v[2:3]
	v_lshl_add_u64 v[10:11], s[2:3], 0, v[2:3]
	v_bfe_u32 v2, v0, 1, 3
	v_and_b32_e32 v9, 15, v0
	v_lshlrev_b32_e32 v6, 4, v1
	v_mov_b32_e32 v7, v3
	v_xor_b32_e32 v17, v12, v2
	v_bitop3_b32 v38, v12, v2, 4 bitop3:0x36
	v_lshlrev_b32_e32 v2, 10, v13
	v_lshl_add_u64 v[4:5], v[4:5], 0, v[6:7]
	v_lshl_add_u64 v[6:7], v[10:11], 0, v[6:7]
	v_lshlrev_b32_e32 v10, 7, v9
	v_add_u32_e32 v94, 0, v2
	s_mov_b64 s[0:1], 0x22000
	s_mov_b64 s[14:15], src_shared_base
	v_lshl_or_b32 v62, v14, 13, v10
	v_lshl_add_u64 v[10:11], v[4:5], 0, s[0:1]
	v_lshl_add_u64 v[12:13], v[6:7], 0, s[0:1]
	v_readfirstlane_b32 s22, v94
	s_mov_b32 s0, m0
	s_mov_b32 m0, s22
	s_nop 0
	global_load_lds_dwordx4 v[4:5], off
	s_mov_b32 m0, s0
	v_mov_b32_e32 v95, s15
	s_mov_b64 s[0:1], 0x4000
	v_lshl_add_u64 v[14:15], v[94:95], 0, s[0:1]
	v_lshrrev_b32_e32 v1, 2, v0
	v_readfirstlane_b32 s23, v14
	s_mov_b32 s2, m0
	s_mov_b32 m0, s23
	s_nop 0
	global_load_lds_dwordx4 v[6:7], off
	s_mov_b32 m0, s2
	s_mov_b64 s[2:3], 0x2000
	v_lshl_add_u64 v[14:15], v[94:95], 0, s[2:3]
	v_and_b32_e32 v8, 0x60, v1
	v_readfirstlane_b32 s20, v14
	s_mov_b32 s4, m0
	s_mov_b32 m0, s20
	s_nop 0
	global_load_lds_dwordx4 v[10:11], off
	s_mov_b32 m0, s4
	s_mov_b64 s[4:5], 0x6000
	v_lshl_add_u64 v[10:11], v[94:95], 0, s[4:5]
	v_mov_b32_e32 v11, s15
	v_readfirstlane_b32 s21, v10
	s_mov_b32 s6, m0
	s_mov_b32 m0, s21
	s_nop 0
	global_load_lds_dwordx4 v[12:13], off
	s_mov_b32 m0, s6
	v_add_u32_e32 v10, 0x8000, v94
	s_mov_b64 s[6:7], 0x80
	v_lshl_add_u64 v[12:13], v[4:5], 0, s[6:7]
	v_readfirstlane_b32 s16, v10
	s_mov_b32 s14, m0
	s_mov_b32 m0, s16
	s_nop 0
	global_load_lds_dwordx4 v[12:13], off
	s_mov_b32 m0, s14
	v_lshl_add_u64 v[14:15], v[10:11], 0, s[0:1]
	v_lshl_add_u64 v[12:13], v[6:7], 0, s[6:7]
	v_readfirstlane_b32 s18, v14
	s_mov_b32 s6, m0
	s_mov_b32 m0, s18
	s_nop 0
	global_load_lds_dwordx4 v[12:13], off
	s_mov_b32 m0, s6
	s_mov_b64 s[14:15], 0x22080
	v_lshl_add_u64 v[14:15], v[10:11], 0, s[2:3]
	v_lshl_add_u64 v[12:13], v[4:5], 0, s[14:15]
	v_readfirstlane_b32 s6, v14
	s_mov_b32 s7, m0
	s_mov_b32 m0, s6
	s_nop 0
	global_load_lds_dwordx4 v[12:13], off
	s_mov_b32 m0, s7
	v_lshl_add_u64 v[10:11], v[10:11], 0, s[4:5]
	s_add_i32 s26, 0, 0x10000
	v_or_b32_e32 v16, v8, v9
	v_lshl_add_u64 v[12:13], v[6:7], 0, s[14:15]
	v_readfirstlane_b32 s14, v10
	s_mov_b32 s7, m0
	s_mov_b32 m0, s14
	s_nop 0
	global_load_lds_dwordx4 v[12:13], off
	s_mov_b32 m0, s7
	v_add_u32_e32 v10, s26, v2
	v_mov_b32_e32 v11, v95
	s_mov_b64 s[24:25], 0x100
	v_lshlrev_b32_e32 v102, 7, v16
	v_lshl_add_u64 v[12:13], v[4:5], 0, s[24:25]
	v_readfirstlane_b32 s7, v10
	v_lshl_add_u64 v[10:11], v[10:11], 0, s[0:1]
	v_lshlrev_b32_e32 v103, 4, v17
	s_mov_b32 s15, m0
	s_mov_b32 m0, s7
	s_nop 0
	global_load_lds_dwordx4 v[12:13], off
	s_mov_b32 m0, s15
	v_lshl_add_u64 v[12:13], v[6:7], 0, s[24:25]
	v_add_u32_e32 v11, 0, v102
	v_add_u32_e32 v46, 0, v62
	v_add_u32_e32 v106, 0x10000, v94
	v_mov_b32_e32 v107, v95
	s_mov_b64 s[24:25], 0x22100
	v_readfirstlane_b32 s7, v10
	s_mov_b32 s15, m0
	s_mov_b32 m0, s7
	s_nop 0
	global_load_lds_dwordx4 v[12:13], off
	s_mov_b32 m0, s15
	v_add_u32_e32 v2, v11, v103
	v_add_u32_e32 v10, v46, v103
	v_lshlrev_b32_e32 v104, 4, v38
	v_lshl_add_u64 v[12:13], v[4:5], 0, s[24:25]
	v_lshl_add_u64 v[38:39], v[106:107], 0, s[2:3]
	s_waitcnt vmcnt(6)
	s_barrier
	ds_read_b128 v[14:17], v2
	ds_read_b128 v[18:21], v2 offset:2048
	ds_read_b128 v[22:25], v10 offset:16384
	ds_read_b128 v[26:29], v10 offset:18432
	ds_read_b128 v[30:33], v10 offset:20480
	ds_read_b128 v[34:37], v10 offset:22528
	v_readfirstlane_b32 s7, v38
	s_mov_b32 s15, m0
	s_mov_b32 m0, s7
	s_nop 0
	global_load_lds_dwordx4 v[12:13], off
	s_mov_b32 m0, s15
	v_lshl_add_u64 v[12:13], v[6:7], 0, s[24:25]
	v_lshl_add_u64 v[38:39], v[106:107], 0, s[4:5]
	v_or_b32_e32 v105, 0x4000, v62
	v_readfirstlane_b32 s15, v38
	s_mov_b32 s17, m0
	s_mov_b32 m0, s15
	s_nop 0
	global_load_lds_dwordx4 v[12:13], off
	s_mov_b32 m0, s17
	v_add_u32_e32 v12, v11, v104
	v_add_u32_e32 v11, v46, v104
	ds_read_b128 v[38:41], v12
	ds_read_b128 v[42:45], v12 offset:2048
	ds_read_b128 v[46:49], v11 offset:16384
	ds_read_b128 v[50:53], v11 offset:18432
	ds_read_b128 v[54:57], v11 offset:20480
	ds_read_b128 v[58:61], v11 offset:22528
	s_waitcnt lgkmcnt(9)
	v_mfma_f32_16x16x32_f16 v[62:65], v[14:17], v[22:25], 0
	s_waitcnt lgkmcnt(8)
	v_mfma_f32_16x16x32_f16 v[66:69], v[14:17], v[26:29], 0
	s_waitcnt lgkmcnt(7)
	v_mfma_f32_16x16x32_f16 v[70:73], v[14:17], v[30:33], 0
	s_waitcnt lgkmcnt(6)
	v_mfma_f32_16x16x32_f16 v[14:17], v[14:17], v[34:37], 0
	v_mfma_f32_16x16x32_f16 v[22:25], v[18:21], v[22:25], 0
	v_mfma_f32_16x16x32_f16 v[26:29], v[18:21], v[26:29], 0
	v_mfma_f32_16x16x32_f16 v[30:33], v[18:21], v[30:33], 0
	v_mfma_f32_16x16x32_f16 v[18:21], v[18:21], v[34:37], 0
	v_add_u32_e32 v94, 0x18000, v94
	s_mov_b64 s[24:25], 0x180
	s_waitcnt vmcnt(4)
	s_barrier
	v_lshl_add_u64 v[34:35], v[4:5], 0, s[24:25]
	v_readfirstlane_b32 s17, v94
	s_mov_b32 s19, m0
	s_mov_b32 m0, s17
	s_nop 0
	global_load_lds_dwordx4 v[34:35], off
	s_mov_b32 m0, s19
	v_lshl_add_u64 v[36:37], v[94:95], 0, s[0:1]
	v_lshl_add_u64 v[34:35], v[6:7], 0, s[24:25]
	v_readfirstlane_b32 s19, v36
	s_mov_b32 s24, m0
	s_mov_b32 m0, s19
	s_nop 0
	global_load_lds_dwordx4 v[34:35], off
	s_mov_b32 m0, s24
	ds_read_b128 v[34:37], v2 offset:32768
	ds_read_b128 v[74:77], v2 offset:34816
	ds_read_b128 v[78:81], v10 offset:49152
	ds_read_b128 v[82:85], v10 offset:51200
	ds_read_b128 v[86:89], v10 offset:53248
	ds_read_b128 v[90:93], v10 offset:55296
	s_waitcnt lgkmcnt(9)
	v_mfma_f32_16x16x32_f16 v[62:65], v[38:41], v[46:49], v[62:65]
	s_waitcnt lgkmcnt(8)
	v_mfma_f32_16x16x32_f16 v[66:69], v[38:41], v[50:53], v[66:69]
	s_waitcnt lgkmcnt(7)
	v_mfma_f32_16x16x32_f16 v[70:73], v[38:41], v[54:57], v[70:73]
	s_waitcnt lgkmcnt(6)
	v_mfma_f32_16x16x32_f16 v[14:17], v[38:41], v[58:61], v[14:17]
	v_mfma_f32_16x16x32_f16 v[22:25], v[42:45], v[46:49], v[22:25]
	v_mfma_f32_16x16x32_f16 v[26:29], v[42:45], v[50:53], v[26:29]
	v_mfma_f32_16x16x32_f16 v[30:33], v[42:45], v[54:57], v[30:33]
	v_mfma_f32_16x16x32_f16 v[18:21], v[42:45], v[58:61], v[18:21]
	s_mov_b64 s[24:25], 0x22180
	v_lshl_add_u64 v[40:41], v[94:95], 0, s[2:3]
	v_lshl_add_u64 v[38:39], v[4:5], 0, s[24:25]
	v_readfirstlane_b32 s2, v40
	s_mov_b32 s3, m0
	s_mov_b32 m0, s2
	s_nop 0
	global_load_lds_dwordx4 v[38:39], off
	s_mov_b32 m0, s3
	v_lshl_add_u64 v[40:41], v[94:95], 0, s[4:5]
	v_lshl_add_u64 v[38:39], v[6:7], 0, s[24:25]
	v_readfirstlane_b32 s3, v40
	s_mov_b32 s4, m0
	s_mov_b32 m0, s3
	s_nop 0
	global_load_lds_dwordx4 v[38:39], off
	s_mov_b32 m0, s4
	ds_read_b128 v[38:41], v12 offset:32768
	ds_read_b128 v[42:45], v12 offset:34816
	ds_read_b128 v[46:49], v11 offset:49152
	ds_read_b128 v[50:53], v11 offset:51200
	ds_read_b128 v[54:57], v11 offset:53248
	ds_read_b128 v[58:61], v11 offset:55296
	s_waitcnt lgkmcnt(9)
	v_mfma_f32_16x16x32_f16 v[62:65], v[34:37], v[78:81], v[62:65]
	s_waitcnt lgkmcnt(8)
	v_mfma_f32_16x16x32_f16 v[66:69], v[34:37], v[82:85], v[66:69]
	s_waitcnt lgkmcnt(7)
	v_mfma_f32_16x16x32_f16 v[70:73], v[34:37], v[86:89], v[70:73]
	s_waitcnt lgkmcnt(6)
	v_mfma_f32_16x16x32_f16 v[34:37], v[34:37], v[90:93], v[14:17]
	v_mfma_f32_16x16x32_f16 v[22:25], v[74:77], v[78:81], v[22:25]
	v_mfma_f32_16x16x32_f16 v[26:29], v[74:77], v[82:85], v[26:29]
	v_mfma_f32_16x16x32_f16 v[30:33], v[74:77], v[86:89], v[30:33]
	v_mfma_f32_16x16x32_f16 v[16:19], v[74:77], v[90:93], v[18:21]
	s_mov_b64 s[4:5], 0x200
	v_lshl_add_u64 v[14:15], v[4:5], 0, s[4:5]
	s_waitcnt vmcnt(4)
	s_barrier
	s_mov_b32 s24, m0
	s_mov_b32 m0, s22
	s_nop 0
	global_load_lds_dwordx4 v[14:15], off
	s_mov_b32 m0, s24
	v_lshl_add_u64 v[14:15], v[6:7], 0, s[4:5]
	s_mov_b32 s4, m0
	s_mov_b32 m0, s23
	s_nop 0
	global_load_lds_dwordx4 v[14:15], off
	s_mov_b32 m0, s4
	v_add_u32_e32 v15, s26, v102
	v_add_u32_e32 v14, v15, v103
	v_add3_u32 v13, s26, v103, v105
	ds_read_b128 v[74:77], v14
	ds_read_b128 v[78:81], v14 offset:2048
	ds_read_b128 v[82:85], v13
	ds_read_b128 v[86:89], v13 offset:2048
	ds_read_b128 v[90:93], v13 offset:4096
	ds_read_b128 v[94:97], v13 offset:6144
	s_waitcnt lgkmcnt(9)
	v_mfma_f32_16x16x32_f16 v[62:65], v[38:41], v[46:49], v[62:65]
	s_waitcnt lgkmcnt(8)
	v_mfma_f32_16x16x32_f16 v[66:69], v[38:41], v[50:53], v[66:69]
	s_waitcnt lgkmcnt(7)
	v_mfma_f32_16x16x32_f16 v[70:73], v[38:41], v[54:57], v[70:73]
	s_waitcnt lgkmcnt(6)
	v_mfma_f32_16x16x32_f16 v[34:37], v[38:41], v[58:61], v[34:37]
	v_mfma_f32_16x16x32_f16 v[20:23], v[42:45], v[46:49], v[22:25]
	v_mfma_f32_16x16x32_f16 v[24:27], v[42:45], v[50:53], v[26:29]
	v_mfma_f32_16x16x32_f16 v[28:31], v[42:45], v[54:57], v[30:33]
	v_mfma_f32_16x16x32_f16 v[38:41], v[42:45], v[58:61], v[16:19]
	s_mov_b64 s[4:5], 0x22200
	s_nop 1
	v_lshl_add_u64 v[16:17], v[4:5], 0, s[4:5]
	s_mov_b32 s24, m0
	s_mov_b32 m0, s20
	s_nop 0
	global_load_lds_dwordx4 v[16:17], off
	s_mov_b32 m0, s24
	v_lshl_add_u64 v[16:17], v[6:7], 0, s[4:5]
	s_mov_b32 s4, m0
	s_mov_b32 m0, s21
	s_nop 0
	global_load_lds_dwordx4 v[16:17], off
	s_mov_b32 m0, s4
	v_add_u32_e32 v16, v15, v104
	v_add3_u32 v15, s26, v104, v105
	ds_read_b128 v[42:45], v16
	ds_read_b128 v[46:49], v16 offset:2048
	ds_read_b128 v[50:53], v15
	ds_read_b128 v[54:57], v15 offset:2048
	ds_read_b128 v[58:61], v15 offset:4096
	ds_read_b128 v[98:101], v15 offset:6144
	s_waitcnt lgkmcnt(9)
	v_mfma_f32_16x16x32_f16 v[62:65], v[74:77], v[82:85], v[62:65]
	s_waitcnt lgkmcnt(8)
	v_mfma_f32_16x16x32_f16 v[66:69], v[74:77], v[86:89], v[66:69]
	s_waitcnt lgkmcnt(7)
	v_mfma_f32_16x16x32_f16 v[70:73], v[74:77], v[90:93], v[70:73]
	s_waitcnt lgkmcnt(6)
	v_mfma_f32_16x16x32_f16 v[32:35], v[74:77], v[94:97], v[34:37]
	v_mfma_f32_16x16x32_f16 v[20:23], v[78:81], v[82:85], v[20:23]
	v_mfma_f32_16x16x32_f16 v[24:27], v[78:81], v[86:89], v[24:27]
	v_mfma_f32_16x16x32_f16 v[28:31], v[78:81], v[90:93], v[28:31]
	v_mfma_f32_16x16x32_f16 v[36:39], v[78:81], v[94:97], v[38:41]
	s_mov_b64 s[4:5], 0x280
	s_waitcnt vmcnt(4)
	s_barrier
	v_lshl_add_u64 v[18:19], v[4:5], 0, s[4:5]
	s_mov_b32 s24, m0
	s_mov_b32 m0, s16
	s_nop 0
	global_load_lds_dwordx4 v[18:19], off
	s_mov_b32 m0, s24
	v_lshl_add_u64 v[18:19], v[6:7], 0, s[4:5]
	s_add_i32 s24, 0, 0x18000
	s_mov_b32 s4, m0
	s_mov_b32 m0, s18
	s_nop 0
	global_load_lds_dwordx4 v[18:19], off
	s_mov_b32 m0, s4
	v_add_u32_e32 v19, s24, v102
	v_add_u32_e32 v17, v19, v103
	v_add3_u32 v18, s24, v103, v105
	ds_read_b128 v[74:77], v17
	ds_read_b128 v[78:81], v17 offset:2048
	ds_read_b128 v[82:85], v18
	ds_read_b128 v[86:89], v18 offset:2048
	ds_read_b128 v[90:93], v18 offset:4096
	ds_read_b128 v[94:97], v18 offset:6144
	s_waitcnt lgkmcnt(9)
	v_mfma_f32_16x16x32_f16 v[62:65], v[42:45], v[50:53], v[62:65]
	s_waitcnt lgkmcnt(8)
	v_mfma_f32_16x16x32_f16 v[66:69], v[42:45], v[54:57], v[66:69]
	s_waitcnt lgkmcnt(7)
	v_mfma_f32_16x16x32_f16 v[70:73], v[42:45], v[58:61], v[70:73]
	s_waitcnt lgkmcnt(6)
	v_mfma_f32_16x16x32_f16 v[32:35], v[42:45], v[98:101], v[32:35]
	v_mfma_f32_16x16x32_f16 v[40:43], v[46:49], v[50:53], v[20:23]
	v_mfma_f32_16x16x32_f16 v[22:25], v[46:49], v[54:57], v[24:27]
	v_mfma_f32_16x16x32_f16 v[26:29], v[46:49], v[58:61], v[28:31]
	v_mfma_f32_16x16x32_f16 v[36:39], v[46:49], v[98:101], v[36:39]
	s_mov_b64 s[4:5], 0x22280
	v_lshl_add_u64 v[20:21], v[4:5], 0, s[4:5]
	s_mov_b32 s25, m0
	s_mov_b32 m0, s6
	s_nop 0
	global_load_lds_dwordx4 v[20:21], off
	s_mov_b32 m0, s25
	v_lshl_add_u64 v[20:21], v[6:7], 0, s[4:5]
	s_mov_b32 s4, m0
	s_mov_b32 m0, s14
	s_nop 0
	global_load_lds_dwordx4 v[20:21], off
	s_mov_b32 m0, s4
	v_add_u32_e32 v19, v19, v104
	v_add3_u32 v20, s24, v104, v105
	ds_read_b128 v[44:47], v19
	ds_read_b128 v[48:51], v19 offset:2048
	ds_read_b128 v[52:55], v20
	ds_read_b128 v[56:59], v20 offset:2048
	ds_read_b128 v[98:101], v20 offset:4096
	ds_read_b128 v[102:105], v20 offset:6144
	s_waitcnt lgkmcnt(9)
	v_mfma_f32_16x16x32_f16 v[60:63], v[74:77], v[82:85], v[62:65]
	s_waitcnt lgkmcnt(8)
	v_mfma_f32_16x16x32_f16 v[64:67], v[74:77], v[86:89], v[66:69]
	s_waitcnt lgkmcnt(7)
	v_mfma_f32_16x16x32_f16 v[68:71], v[74:77], v[90:93], v[70:73]
	s_waitcnt lgkmcnt(6)
	v_mfma_f32_16x16x32_f16 v[30:33], v[74:77], v[94:97], v[32:35]
	v_mfma_f32_16x16x32_f16 v[40:43], v[78:81], v[82:85], v[40:43]
	v_mfma_f32_16x16x32_f16 v[22:25], v[78:81], v[86:89], v[22:25]
	v_mfma_f32_16x16x32_f16 v[26:29], v[78:81], v[90:93], v[26:29]
	v_mfma_f32_16x16x32_f16 v[34:37], v[78:81], v[94:97], v[36:39]
	s_mov_b64 s[24:25], 0x300
	s_waitcnt vmcnt(4)
	s_barrier
	s_nop 0
	v_lshl_add_u64 v[38:39], v[4:5], 0, s[24:25]
	v_readfirstlane_b32 s4, v106
	s_mov_b32 s5, m0
	s_mov_b32 m0, s4
	s_nop 0
	global_load_lds_dwordx4 v[38:39], off
	s_mov_b32 m0, s5
	v_lshl_add_u64 v[72:73], v[106:107], 0, s[0:1]
	v_lshl_add_u64 v[38:39], v[6:7], 0, s[24:25]
	v_readfirstlane_b32 s0, v72
	s_mov_b32 s1, m0
	s_mov_b32 m0, s0
	s_nop 0
	global_load_lds_dwordx4 v[38:39], off
	s_mov_b32 m0, s1
	ds_read_b128 v[72:75], v2
	ds_read_b128 v[76:79], v2 offset:2048
	ds_read_b128 v[80:83], v10 offset:16384
	ds_read_b128 v[84:87], v10 offset:18432
	ds_read_b128 v[88:91], v10 offset:20480
	ds_read_b128 v[92:95], v10 offset:22528
	s_waitcnt lgkmcnt(9)
	v_mfma_f32_16x16x32_f16 v[60:63], v[44:47], v[52:55], v[60:63]
	s_waitcnt lgkmcnt(8)
	v_mfma_f32_16x16x32_f16 v[64:67], v[44:47], v[56:59], v[64:67]
	s_waitcnt lgkmcnt(7)
	v_mfma_f32_16x16x32_f16 v[68:71], v[44:47], v[98:101], v[68:71]
	s_waitcnt lgkmcnt(6)
	v_mfma_f32_16x16x32_f16 v[30:33], v[44:47], v[102:105], v[30:33]
	v_mfma_f32_16x16x32_f16 v[38:41], v[48:51], v[52:55], v[40:43]
	v_mfma_f32_16x16x32_f16 v[22:25], v[48:51], v[56:59], v[22:25]
	v_mfma_f32_16x16x32_f16 v[26:29], v[48:51], v[98:101], v[26:29]
	v_mfma_f32_16x16x32_f16 v[34:37], v[48:51], v[102:105], v[34:37]
	s_mov_b64 s[24:25], 0x22300
	v_lshl_add_u64 v[42:43], v[4:5], 0, s[24:25]
	s_mov_b32 s1, m0
	s_mov_b32 m0, s7
	s_nop 0
	global_load_lds_dwordx4 v[42:43], off
	s_mov_b32 m0, s1
	v_lshl_add_u64 v[42:43], v[6:7], 0, s[24:25]
	s_mov_b32 s1, m0
	s_mov_b32 m0, s15
	s_nop 0
	global_load_lds_dwordx4 v[42:43], off
	s_mov_b32 m0, s1
	ds_read_b128 v[42:45], v12
	ds_read_b128 v[46:49], v12 offset:2048
	ds_read_b128 v[50:53], v11 offset:16384
	ds_read_b128 v[54:57], v11 offset:18432
	ds_read_b128 v[96:99], v11 offset:20480
	ds_read_b128 v[100:103], v11 offset:22528
	s_waitcnt lgkmcnt(9)
	v_mfma_f32_16x16x32_f16 v[58:61], v[72:75], v[80:83], v[60:63]
	s_waitcnt lgkmcnt(8)
	v_mfma_f32_16x16x32_f16 v[62:65], v[72:75], v[84:87], v[64:67]
	s_waitcnt lgkmcnt(7)
	v_mfma_f32_16x16x32_f16 v[66:69], v[72:75], v[88:91], v[68:71]
	s_waitcnt lgkmcnt(6)
	v_mfma_f32_16x16x32_f16 v[30:33], v[72:75], v[92:95], v[30:33]
	v_mfma_f32_16x16x32_f16 v[38:41], v[76:79], v[80:83], v[38:41]
	v_mfma_f32_16x16x32_f16 v[22:25], v[76:79], v[84:87], v[22:25]
	v_mfma_f32_16x16x32_f16 v[26:29], v[76:79], v[88:91], v[26:29]
	v_mfma_f32_16x16x32_f16 v[34:37], v[76:79], v[92:95], v[34:37]
	s_mov_b64 s[24:25], 0x380
	s_waitcnt vmcnt(4)
	s_barrier
	v_lshl_add_u64 v[70:71], v[4:5], 0, s[24:25]
	s_mov_b32 s1, m0
	s_mov_b32 m0, s17
	s_nop 0
	global_load_lds_dwordx4 v[70:71], off
	s_mov_b32 m0, s1
	v_lshl_add_u64 v[70:71], v[6:7], 0, s[24:25]
	s_mov_b32 s1, m0
	s_mov_b32 m0, s19
	s_nop 0
	global_load_lds_dwordx4 v[70:71], off
	s_mov_b32 m0, s1
	ds_read_b128 v[70:73], v2 offset:32768
	ds_read_b128 v[74:77], v2 offset:34816
	ds_read_b128 v[78:81], v10 offset:49152
	ds_read_b128 v[82:85], v10 offset:51200
	ds_read_b128 v[86:89], v10 offset:53248
	ds_read_b128 v[90:93], v10 offset:55296
	s_waitcnt lgkmcnt(9)
	v_mfma_f32_16x16x32_f16 v[58:61], v[42:45], v[50:53], v[58:61]
	s_waitcnt lgkmcnt(8)
	v_mfma_f32_16x16x32_f16 v[62:65], v[42:45], v[54:57], v[62:65]
	s_waitcnt lgkmcnt(7)
	v_mfma_f32_16x16x32_f16 v[66:69], v[42:45], v[96:99], v[66:69]
	s_waitcnt lgkmcnt(6)
	v_mfma_f32_16x16x32_f16 v[30:33], v[42:45], v[100:103], v[30:33]
	v_mfma_f32_16x16x32_f16 v[38:41], v[46:49], v[50:53], v[38:41]
	v_mfma_f32_16x16x32_f16 v[22:25], v[46:49], v[54:57], v[22:25]
	v_mfma_f32_16x16x32_f16 v[26:29], v[46:49], v[96:99], v[26:29]
	v_mfma_f32_16x16x32_f16 v[34:37], v[46:49], v[100:103], v[34:37]
	s_mov_b64 s[24:25], 0x22380
	v_lshl_add_u64 v[42:43], v[4:5], 0, s[24:25]
	s_mov_b32 s1, m0
	s_mov_b32 m0, s2
	s_nop 0
	global_load_lds_dwordx4 v[42:43], off
	s_mov_b32 m0, s1
	v_lshl_add_u64 v[42:43], v[6:7], 0, s[24:25]
	s_mov_b32 s1, m0
	s_mov_b32 m0, s3
	s_nop 0
	global_load_lds_dwordx4 v[42:43], off
	s_mov_b32 m0, s1
	ds_read_b128 v[42:45], v12 offset:32768
	ds_read_b128 v[46:49], v12 offset:34816
	ds_read_b128 v[50:53], v11 offset:49152
	ds_read_b128 v[54:57], v11 offset:51200
	ds_read_b128 v[94:97], v11 offset:53248
	ds_read_b128 v[98:101], v11 offset:55296
	s_waitcnt lgkmcnt(9)
	v_mfma_f32_16x16x32_f16 v[58:61], v[70:73], v[78:81], v[58:61]
	s_waitcnt lgkmcnt(8)
	v_mfma_f32_16x16x32_f16 v[62:65], v[70:73], v[82:85], v[62:65]
	s_waitcnt lgkmcnt(7)
	v_mfma_f32_16x16x32_f16 v[66:69], v[70:73], v[86:89], v[66:69]
	s_waitcnt lgkmcnt(6)
	v_mfma_f32_16x16x32_f16 v[30:33], v[70:73], v[90:93], v[30:33]
	v_mfma_f32_16x16x32_f16 v[38:41], v[74:77], v[78:81], v[38:41]
	v_mfma_f32_16x16x32_f16 v[22:25], v[74:77], v[82:85], v[22:25]
	v_mfma_f32_16x16x32_f16 v[26:29], v[74:77], v[86:89], v[26:29]
	v_mfma_f32_16x16x32_f16 v[34:37], v[74:77], v[90:93], v[34:37]
	s_mov_b64 s[24:25], 0x400
	s_waitcnt vmcnt(4)
	s_barrier
	v_lshl_add_u64 v[70:71], v[4:5], 0, s[24:25]
	s_mov_b32 s1, m0
	s_mov_b32 m0, s22
	s_nop 0
	global_load_lds_dwordx4 v[70:71], off
	s_mov_b32 m0, s1
	v_lshl_add_u64 v[70:71], v[6:7], 0, s[24:25]
	s_mov_b32 s1, m0
	s_mov_b32 m0, s23
	s_nop 0
	global_load_lds_dwordx4 v[70:71], off
	s_mov_b32 m0, s1
	ds_read_b128 v[70:73], v14
	ds_read_b128 v[74:77], v14 offset:2048
	ds_read_b128 v[78:81], v13
	ds_read_b128 v[82:85], v13 offset:2048
	ds_read_b128 v[86:89], v13 offset:4096
	ds_read_b128 v[90:93], v13 offset:6144
	s_waitcnt lgkmcnt(9)
	v_mfma_f32_16x16x32_f16 v[58:61], v[42:45], v[50:53], v[58:61]
	s_waitcnt lgkmcnt(8)
	v_mfma_f32_16x16x32_f16 v[62:65], v[42:45], v[54:57], v[62:65]
	s_waitcnt lgkmcnt(7)
	v_mfma_f32_16x16x32_f16 v[66:69], v[42:45], v[94:97], v[66:69]
	s_waitcnt lgkmcnt(6)
	v_mfma_f32_16x16x32_f16 v[30:33], v[42:45], v[98:101], v[30:33]
	v_mfma_f32_16x16x32_f16 v[38:41], v[46:49], v[50:53], v[38:41]
	v_mfma_f32_16x16x32_f16 v[22:25], v[46:49], v[54:57], v[22:25]
	v_mfma_f32_16x16x32_f16 v[26:29], v[46:49], v[94:97], v[26:29]
	v_mfma_f32_16x16x32_f16 v[34:37], v[46:49], v[98:101], v[34:37]
	s_mov_b64 s[24:25], 0x22400
	v_lshl_add_u64 v[42:43], v[4:5], 0, s[24:25]
	s_mov_b32 s1, m0
	s_mov_b32 m0, s20
	s_nop 0
	global_load_lds_dwordx4 v[42:43], off
	s_mov_b32 m0, s1
	v_lshl_add_u64 v[42:43], v[6:7], 0, s[24:25]
	s_mov_b32 s1, m0
	s_mov_b32 m0, s21
	s_nop 0
	global_load_lds_dwordx4 v[42:43], off
	s_mov_b32 m0, s1
	ds_read_b128 v[42:45], v16
	ds_read_b128 v[46:49], v16 offset:2048
	ds_read_b128 v[50:53], v15
	ds_read_b128 v[54:57], v15 offset:2048
	ds_read_b128 v[94:97], v15 offset:4096
	ds_read_b128 v[98:101], v15 offset:6144
	s_waitcnt lgkmcnt(9)
	v_mfma_f32_16x16x32_f16 v[58:61], v[70:73], v[78:81], v[58:61]
	s_waitcnt lgkmcnt(8)
	v_mfma_f32_16x16x32_f16 v[62:65], v[70:73], v[82:85], v[62:65]
	s_waitcnt lgkmcnt(7)
	v_mfma_f32_16x16x32_f16 v[66:69], v[70:73], v[86:89], v[66:69]
	s_waitcnt lgkmcnt(6)
	v_mfma_f32_16x16x32_f16 v[30:33], v[70:73], v[90:93], v[30:33]
	v_mfma_f32_16x16x32_f16 v[38:41], v[74:77], v[78:81], v[38:41]
	v_mfma_f32_16x16x32_f16 v[22:25], v[74:77], v[82:85], v[22:25]
	v_mfma_f32_16x16x32_f16 v[26:29], v[74:77], v[86:89], v[26:29]
	v_mfma_f32_16x16x32_f16 v[34:37], v[74:77], v[90:93], v[34:37]
	s_mov_b64 s[24:25], 0x480
	s_waitcnt vmcnt(4)
	s_barrier
	v_lshl_add_u64 v[70:71], v[4:5], 0, s[24:25]
	s_mov_b32 s1, m0
	s_mov_b32 m0, s16
	s_nop 0
	global_load_lds_dwordx4 v[70:71], off
	s_mov_b32 m0, s1
	v_lshl_add_u64 v[70:71], v[6:7], 0, s[24:25]
	s_mov_b32 s1, m0
	s_mov_b32 m0, s18
	s_nop 0
	global_load_lds_dwordx4 v[70:71], off
	s_mov_b32 m0, s1
	ds_read_b128 v[70:73], v17
	ds_read_b128 v[74:77], v17 offset:2048
	ds_read_b128 v[78:81], v18
	ds_read_b128 v[82:85], v18 offset:2048
	ds_read_b128 v[86:89], v18 offset:4096
	ds_read_b128 v[90:93], v18 offset:6144
	s_waitcnt lgkmcnt(9)
	v_mfma_f32_16x16x32_f16 v[58:61], v[42:45], v[50:53], v[58:61]
	s_waitcnt lgkmcnt(8)
	v_mfma_f32_16x16x32_f16 v[62:65], v[42:45], v[54:57], v[62:65]
	s_waitcnt lgkmcnt(7)
	v_mfma_f32_16x16x32_f16 v[66:69], v[42:45], v[94:97], v[66:69]
	s_waitcnt lgkmcnt(6)
	v_mfma_f32_16x16x32_f16 v[30:33], v[42:45], v[98:101], v[30:33]
	v_mfma_f32_16x16x32_f16 v[38:41], v[46:49], v[50:53], v[38:41]
	v_mfma_f32_16x16x32_f16 v[22:25], v[46:49], v[54:57], v[22:25]
	v_mfma_f32_16x16x32_f16 v[26:29], v[46:49], v[94:97], v[26:29]
	v_mfma_f32_16x16x32_f16 v[34:37], v[46:49], v[98:101], v[34:37]
	s_mov_b64 s[24:25], 0x22480
	v_lshl_add_u64 v[42:43], v[4:5], 0, s[24:25]
	s_mov_b32 s1, m0
	s_mov_b32 m0, s6
	s_nop 0
	global_load_lds_dwordx4 v[42:43], off
	s_mov_b32 m0, s1
	v_lshl_add_u64 v[42:43], v[6:7], 0, s[24:25]
	s_mov_b32 s1, m0
	s_mov_b32 m0, s14
	s_nop 0
	global_load_lds_dwordx4 v[42:43], off
	s_mov_b32 m0, s1
	ds_read_b128 v[42:45], v19
	ds_read_b128 v[46:49], v19 offset:2048
	ds_read_b128 v[50:53], v20
	ds_read_b128 v[54:57], v20 offset:2048
	ds_read_b128 v[94:97], v20 offset:4096
	ds_read_b128 v[98:101], v20 offset:6144
	s_waitcnt lgkmcnt(9)
	v_mfma_f32_16x16x32_f16 v[58:61], v[70:73], v[78:81], v[58:61]
	s_waitcnt lgkmcnt(8)
	v_mfma_f32_16x16x32_f16 v[62:65], v[70:73], v[82:85], v[62:65]
	s_waitcnt lgkmcnt(7)
	v_mfma_f32_16x16x32_f16 v[66:69], v[70:73], v[86:89], v[66:69]
	s_waitcnt lgkmcnt(6)
	v_mfma_f32_16x16x32_f16 v[30:33], v[70:73], v[90:93], v[30:33]
	v_mfma_f32_16x16x32_f16 v[38:41], v[74:77], v[78:81], v[38:41]
	v_mfma_f32_16x16x32_f16 v[22:25], v[74:77], v[82:85], v[22:25]
	v_mfma_f32_16x16x32_f16 v[26:29], v[74:77], v[86:89], v[26:29]
	v_mfma_f32_16x16x32_f16 v[34:37], v[74:77], v[90:93], v[34:37]
	s_mov_b64 s[24:25], 0x500
	s_waitcnt vmcnt(4)
	s_barrier
	v_lshl_add_u64 v[70:71], v[4:5], 0, s[24:25]
	s_mov_b32 s1, m0
	s_mov_b32 m0, s4
	s_nop 0
	global_load_lds_dwordx4 v[70:71], off
	s_mov_b32 m0, s1
	v_lshl_add_u64 v[70:71], v[6:7], 0, s[24:25]
	s_mov_b32 s1, m0
	s_mov_b32 m0, s0
	s_nop 0
	global_load_lds_dwordx4 v[70:71], off
	s_mov_b32 m0, s1
	ds_read_b128 v[70:73], v2
	ds_read_b128 v[74:77], v2 offset:2048
	ds_read_b128 v[78:81], v10 offset:16384
	ds_read_b128 v[82:85], v10 offset:18432
	ds_read_b128 v[86:89], v10 offset:20480
	ds_read_b128 v[90:93], v10 offset:22528
	s_waitcnt lgkmcnt(9)
	v_mfma_f32_16x16x32_f16 v[58:61], v[42:45], v[50:53], v[58:61]
	s_waitcnt lgkmcnt(8)
	v_mfma_f32_16x16x32_f16 v[62:65], v[42:45], v[54:57], v[62:65]
	s_waitcnt lgkmcnt(7)
	v_mfma_f32_16x16x32_f16 v[66:69], v[42:45], v[94:97], v[66:69]
	s_waitcnt lgkmcnt(6)
	v_mfma_f32_16x16x32_f16 v[30:33], v[42:45], v[98:101], v[30:33]
	v_mfma_f32_16x16x32_f16 v[38:41], v[46:49], v[50:53], v[38:41]
	v_mfma_f32_16x16x32_f16 v[22:25], v[46:49], v[54:57], v[22:25]
	v_mfma_f32_16x16x32_f16 v[26:29], v[46:49], v[94:97], v[26:29]
	v_mfma_f32_16x16x32_f16 v[34:37], v[46:49], v[98:101], v[34:37]
	s_mov_b64 s[24:25], 0x22500
	v_lshl_add_u64 v[42:43], v[4:5], 0, s[24:25]
	s_mov_b32 s1, m0
	s_mov_b32 m0, s7
	s_nop 0
	global_load_lds_dwordx4 v[42:43], off
	s_mov_b32 m0, s1
	v_lshl_add_u64 v[42:43], v[6:7], 0, s[24:25]
	s_mov_b32 s1, m0
	s_mov_b32 m0, s15
	s_nop 0
	global_load_lds_dwordx4 v[42:43], off
	s_mov_b32 m0, s1
	ds_read_b128 v[42:45], v12
	ds_read_b128 v[46:49], v12 offset:2048
	ds_read_b128 v[50:53], v11 offset:16384
	ds_read_b128 v[54:57], v11 offset:18432
	ds_read_b128 v[94:97], v11 offset:20480
	ds_read_b128 v[98:101], v11 offset:22528
	s_waitcnt lgkmcnt(9)
	v_mfma_f32_16x16x32_f16 v[58:61], v[70:73], v[78:81], v[58:61]
	s_waitcnt lgkmcnt(8)
	v_mfma_f32_16x16x32_f16 v[62:65], v[70:73], v[82:85], v[62:65]
	s_waitcnt lgkmcnt(7)
	v_mfma_f32_16x16x32_f16 v[66:69], v[70:73], v[86:89], v[66:69]
	s_waitcnt lgkmcnt(6)
	v_mfma_f32_16x16x32_f16 v[30:33], v[70:73], v[90:93], v[30:33]
	v_mfma_f32_16x16x32_f16 v[38:41], v[74:77], v[78:81], v[38:41]
	v_mfma_f32_16x16x32_f16 v[22:25], v[74:77], v[82:85], v[22:25]
	v_mfma_f32_16x16x32_f16 v[26:29], v[74:77], v[86:89], v[26:29]
	v_mfma_f32_16x16x32_f16 v[34:37], v[74:77], v[90:93], v[34:37]
	s_mov_b64 s[24:25], 0x580
	s_waitcnt vmcnt(4)
	s_barrier
	v_lshl_add_u64 v[70:71], v[4:5], 0, s[24:25]
	s_mov_b32 s1, m0
	s_mov_b32 m0, s17
	s_nop 0
	global_load_lds_dwordx4 v[70:71], off
	s_mov_b32 m0, s1
	v_lshl_add_u64 v[70:71], v[6:7], 0, s[24:25]
	s_mov_b32 s1, m0
	s_mov_b32 m0, s19
	s_nop 0
	global_load_lds_dwordx4 v[70:71], off
	s_mov_b32 m0, s1
	ds_read_b128 v[70:73], v2 offset:32768
	ds_read_b128 v[74:77], v2 offset:34816
	ds_read_b128 v[78:81], v10 offset:49152
	ds_read_b128 v[82:85], v10 offset:51200
	ds_read_b128 v[86:89], v10 offset:53248
	ds_read_b128 v[90:93], v10 offset:55296
	s_waitcnt lgkmcnt(9)
	v_mfma_f32_16x16x32_f16 v[58:61], v[42:45], v[50:53], v[58:61]
	s_waitcnt lgkmcnt(8)
	v_mfma_f32_16x16x32_f16 v[62:65], v[42:45], v[54:57], v[62:65]
	s_waitcnt lgkmcnt(7)
	v_mfma_f32_16x16x32_f16 v[66:69], v[42:45], v[94:97], v[66:69]
	s_waitcnt lgkmcnt(6)
	v_mfma_f32_16x16x32_f16 v[30:33], v[42:45], v[98:101], v[30:33]
	v_mfma_f32_16x16x32_f16 v[38:41], v[46:49], v[50:53], v[38:41]
	v_mfma_f32_16x16x32_f16 v[22:25], v[46:49], v[54:57], v[22:25]
	v_mfma_f32_16x16x32_f16 v[26:29], v[46:49], v[94:97], v[26:29]
	v_mfma_f32_16x16x32_f16 v[34:37], v[46:49], v[98:101], v[34:37]
	s_mov_b64 s[24:25], 0x22580
	v_lshl_add_u64 v[42:43], v[4:5], 0, s[24:25]
	s_mov_b32 s1, m0
	s_mov_b32 m0, s2
	s_nop 0
	global_load_lds_dwordx4 v[42:43], off
	s_mov_b32 m0, s1
	v_lshl_add_u64 v[42:43], v[6:7], 0, s[24:25]
	s_mov_b32 s1, m0
	s_mov_b32 m0, s3
	s_nop 0
	global_load_lds_dwordx4 v[42:43], off
	s_mov_b32 m0, s1
	ds_read_b128 v[42:45], v12 offset:32768
	ds_read_b128 v[46:49], v12 offset:34816
	ds_read_b128 v[50:53], v11 offset:49152
	ds_read_b128 v[54:57], v11 offset:51200
	ds_read_b128 v[94:97], v11 offset:53248
	ds_read_b128 v[98:101], v11 offset:55296
	s_waitcnt lgkmcnt(9)
	v_mfma_f32_16x16x32_f16 v[58:61], v[70:73], v[78:81], v[58:61]
	s_waitcnt lgkmcnt(8)
	v_mfma_f32_16x16x32_f16 v[62:65], v[70:73], v[82:85], v[62:65]
	s_waitcnt lgkmcnt(7)
	v_mfma_f32_16x16x32_f16 v[66:69], v[70:73], v[86:89], v[66:69]
	s_waitcnt lgkmcnt(6)
	v_mfma_f32_16x16x32_f16 v[30:33], v[70:73], v[90:93], v[30:33]
	v_mfma_f32_16x16x32_f16 v[38:41], v[74:77], v[78:81], v[38:41]
	v_mfma_f32_16x16x32_f16 v[22:25], v[74:77], v[82:85], v[22:25]
	v_mfma_f32_16x16x32_f16 v[26:29], v[74:77], v[86:89], v[26:29]
	v_mfma_f32_16x16x32_f16 v[34:37], v[74:77], v[90:93], v[34:37]
	s_mov_b64 s[24:25], 0x600
	s_waitcnt vmcnt(4)
	s_barrier
	v_lshl_add_u64 v[70:71], v[4:5], 0, s[24:25]
	s_mov_b32 s1, m0
	s_mov_b32 m0, s22
	s_nop 0
	global_load_lds_dwordx4 v[70:71], off
	s_mov_b32 m0, s1
	v_lshl_add_u64 v[70:71], v[6:7], 0, s[24:25]
	s_mov_b32 s1, m0
	s_mov_b32 m0, s23
	s_nop 0
	global_load_lds_dwordx4 v[70:71], off
	s_mov_b32 m0, s1
	ds_read_b128 v[70:73], v14
	ds_read_b128 v[74:77], v14 offset:2048
	ds_read_b128 v[78:81], v13
	ds_read_b128 v[82:85], v13 offset:2048
	ds_read_b128 v[86:89], v13 offset:4096
	ds_read_b128 v[90:93], v13 offset:6144
	s_waitcnt lgkmcnt(9)
	v_mfma_f32_16x16x32_f16 v[58:61], v[42:45], v[50:53], v[58:61]
	s_waitcnt lgkmcnt(8)
	v_mfma_f32_16x16x32_f16 v[62:65], v[42:45], v[54:57], v[62:65]
	s_waitcnt lgkmcnt(7)
	v_mfma_f32_16x16x32_f16 v[66:69], v[42:45], v[94:97], v[66:69]
	s_waitcnt lgkmcnt(6)
	v_mfma_f32_16x16x32_f16 v[30:33], v[42:45], v[98:101], v[30:33]
	v_mfma_f32_16x16x32_f16 v[38:41], v[46:49], v[50:53], v[38:41]
	v_mfma_f32_16x16x32_f16 v[22:25], v[46:49], v[54:57], v[22:25]
	v_mfma_f32_16x16x32_f16 v[26:29], v[46:49], v[94:97], v[26:29]
	v_mfma_f32_16x16x32_f16 v[34:37], v[46:49], v[98:101], v[34:37]
	s_mov_b64 s[22:23], 0x22600
	v_lshl_add_u64 v[42:43], v[4:5], 0, s[22:23]
	s_mov_b32 s1, m0
	s_mov_b32 m0, s20
	s_nop 0
	global_load_lds_dwordx4 v[42:43], off
	s_mov_b32 m0, s1
	v_lshl_add_u64 v[42:43], v[6:7], 0, s[22:23]
	s_mov_b32 s1, m0
	s_mov_b32 m0, s21
	s_nop 0
	global_load_lds_dwordx4 v[42:43], off
	s_mov_b32 m0, s1
	ds_read_b128 v[42:45], v16
	ds_read_b128 v[46:49], v16 offset:2048
	ds_read_b128 v[50:53], v15
	ds_read_b128 v[54:57], v15 offset:2048
	ds_read_b128 v[94:97], v15 offset:4096
	ds_read_b128 v[98:101], v15 offset:6144
	s_waitcnt lgkmcnt(9)
	v_mfma_f32_16x16x32_f16 v[58:61], v[70:73], v[78:81], v[58:61]
	s_waitcnt lgkmcnt(8)
	v_mfma_f32_16x16x32_f16 v[62:65], v[70:73], v[82:85], v[62:65]
	s_waitcnt lgkmcnt(7)
	v_mfma_f32_16x16x32_f16 v[66:69], v[70:73], v[86:89], v[66:69]
	s_waitcnt lgkmcnt(6)
	v_mfma_f32_16x16x32_f16 v[30:33], v[70:73], v[90:93], v[30:33]
	v_mfma_f32_16x16x32_f16 v[38:41], v[74:77], v[78:81], v[38:41]
	v_mfma_f32_16x16x32_f16 v[22:25], v[74:77], v[82:85], v[22:25]
	v_mfma_f32_16x16x32_f16 v[26:29], v[74:77], v[86:89], v[26:29]
	v_mfma_f32_16x16x32_f16 v[34:37], v[74:77], v[90:93], v[34:37]
	s_mov_b64 s[20:21], 0x680
	s_waitcnt vmcnt(4)
	s_barrier
	v_lshl_add_u64 v[70:71], v[4:5], 0, s[20:21]
	s_mov_b32 s1, m0
	s_mov_b32 m0, s16
	s_nop 0
	global_load_lds_dwordx4 v[70:71], off
	s_mov_b32 m0, s1
	v_lshl_add_u64 v[70:71], v[6:7], 0, s[20:21]
	s_mov_b32 s1, m0
	s_mov_b32 m0, s18
	s_nop 0
	global_load_lds_dwordx4 v[70:71], off
	s_mov_b32 m0, s1
	ds_read_b128 v[70:73], v17
	ds_read_b128 v[74:77], v17 offset:2048
	ds_read_b128 v[78:81], v18
	ds_read_b128 v[82:85], v18 offset:2048
	ds_read_b128 v[86:89], v18 offset:4096
	ds_read_b128 v[90:93], v18 offset:6144
	s_waitcnt lgkmcnt(9)
	v_mfma_f32_16x16x32_f16 v[58:61], v[42:45], v[50:53], v[58:61]
	s_waitcnt lgkmcnt(8)
	v_mfma_f32_16x16x32_f16 v[62:65], v[42:45], v[54:57], v[62:65]
	s_waitcnt lgkmcnt(7)
	v_mfma_f32_16x16x32_f16 v[66:69], v[42:45], v[94:97], v[66:69]
	s_waitcnt lgkmcnt(6)
	v_mfma_f32_16x16x32_f16 v[30:33], v[42:45], v[98:101], v[30:33]
	v_mfma_f32_16x16x32_f16 v[38:41], v[46:49], v[50:53], v[38:41]
	v_mfma_f32_16x16x32_f16 v[22:25], v[46:49], v[54:57], v[22:25]
	v_mfma_f32_16x16x32_f16 v[26:29], v[46:49], v[94:97], v[26:29]
	v_mfma_f32_16x16x32_f16 v[34:37], v[46:49], v[98:101], v[34:37]
	s_mov_b64 s[20:21], 0x22680
	v_lshl_add_u64 v[42:43], v[4:5], 0, s[20:21]
	s_mov_b32 s1, m0
	s_mov_b32 m0, s6
	s_nop 0
	global_load_lds_dwordx4 v[42:43], off
	s_mov_b32 m0, s1
	v_lshl_add_u64 v[42:43], v[6:7], 0, s[20:21]
	s_mov_b32 s1, m0
	s_mov_b32 m0, s14
	s_nop 0
	global_load_lds_dwordx4 v[42:43], off
	s_mov_b32 m0, s1
	ds_read_b128 v[42:45], v19
	ds_read_b128 v[46:49], v19 offset:2048
	ds_read_b128 v[50:53], v20
	ds_read_b128 v[54:57], v20 offset:2048
	ds_read_b128 v[94:97], v20 offset:4096
	ds_read_b128 v[98:101], v20 offset:6144
	s_waitcnt lgkmcnt(9)
	v_mfma_f32_16x16x32_f16 v[58:61], v[70:73], v[78:81], v[58:61]
	s_waitcnt lgkmcnt(8)
	v_mfma_f32_16x16x32_f16 v[62:65], v[70:73], v[82:85], v[62:65]
	s_waitcnt lgkmcnt(7)
	v_mfma_f32_16x16x32_f16 v[66:69], v[70:73], v[86:89], v[66:69]
	s_waitcnt lgkmcnt(6)
	v_mfma_f32_16x16x32_f16 v[30:33], v[70:73], v[90:93], v[30:33]
	v_mfma_f32_16x16x32_f16 v[38:41], v[74:77], v[78:81], v[38:41]
	v_mfma_f32_16x16x32_f16 v[22:25], v[74:77], v[82:85], v[22:25]
	v_mfma_f32_16x16x32_f16 v[26:29], v[74:77], v[86:89], v[26:29]
	v_mfma_f32_16x16x32_f16 v[34:37], v[74:77], v[90:93], v[34:37]
	s_mov_b64 s[20:21], 0x700
	s_waitcnt vmcnt(4)
	s_barrier
	v_lshl_add_u64 v[70:71], v[4:5], 0, s[20:21]
	s_mov_b32 s1, m0
	s_mov_b32 m0, s4
	s_nop 0
	global_load_lds_dwordx4 v[70:71], off
	s_mov_b32 m0, s1
	v_lshl_add_u64 v[70:71], v[6:7], 0, s[20:21]
	s_mov_b32 s1, m0
	s_mov_b32 m0, s0
	s_nop 0
	global_load_lds_dwordx4 v[70:71], off
	s_mov_b32 m0, s1
	ds_read_b128 v[70:73], v2
	ds_read_b128 v[74:77], v2 offset:2048
	ds_read_b128 v[78:81], v10 offset:16384
	ds_read_b128 v[82:85], v10 offset:18432
	ds_read_b128 v[86:89], v10 offset:20480
	ds_read_b128 v[90:93], v10 offset:22528
	s_waitcnt lgkmcnt(9)
	v_mfma_f32_16x16x32_f16 v[58:61], v[42:45], v[50:53], v[58:61]
	s_waitcnt lgkmcnt(8)
	v_mfma_f32_16x16x32_f16 v[62:65], v[42:45], v[54:57], v[62:65]
	s_waitcnt lgkmcnt(7)
	v_mfma_f32_16x16x32_f16 v[66:69], v[42:45], v[94:97], v[66:69]
	s_waitcnt lgkmcnt(6)
	v_mfma_f32_16x16x32_f16 v[30:33], v[42:45], v[98:101], v[30:33]
	v_mfma_f32_16x16x32_f16 v[38:41], v[46:49], v[50:53], v[38:41]
	v_mfma_f32_16x16x32_f16 v[22:25], v[46:49], v[54:57], v[22:25]
	v_mfma_f32_16x16x32_f16 v[26:29], v[46:49], v[94:97], v[26:29]
	v_mfma_f32_16x16x32_f16 v[34:37], v[46:49], v[98:101], v[34:37]
	s_mov_b64 s[0:1], 0x22700
	v_lshl_add_u64 v[42:43], v[4:5], 0, s[0:1]
	s_mov_b32 s4, m0
	s_mov_b32 m0, s7
	s_nop 0
	global_load_lds_dwordx4 v[42:43], off
	s_mov_b32 m0, s4
	v_lshl_add_u64 v[42:43], v[6:7], 0, s[0:1]
	s_mov_b32 s0, m0
	s_mov_b32 m0, s15
	s_nop 0
	global_load_lds_dwordx4 v[42:43], off
	s_mov_b32 m0, s0
	ds_read_b128 v[42:45], v12
	ds_read_b128 v[46:49], v12 offset:2048
	ds_read_b128 v[50:53], v11 offset:16384
	ds_read_b128 v[54:57], v11 offset:18432
	ds_read_b128 v[94:97], v11 offset:20480
	ds_read_b128 v[98:101], v11 offset:22528
	s_waitcnt lgkmcnt(9)
	v_mfma_f32_16x16x32_f16 v[58:61], v[70:73], v[78:81], v[58:61]
	s_waitcnt lgkmcnt(8)
	v_mfma_f32_16x16x32_f16 v[62:65], v[70:73], v[82:85], v[62:65]
	s_waitcnt lgkmcnt(7)
	v_mfma_f32_16x16x32_f16 v[66:69], v[70:73], v[86:89], v[66:69]
	s_waitcnt lgkmcnt(6)
	v_mfma_f32_16x16x32_f16 v[30:33], v[70:73], v[90:93], v[30:33]
	v_mfma_f32_16x16x32_f16 v[38:41], v[74:77], v[78:81], v[38:41]
	v_mfma_f32_16x16x32_f16 v[22:25], v[74:77], v[82:85], v[22:25]
	v_mfma_f32_16x16x32_f16 v[26:29], v[74:77], v[86:89], v[26:29]
	v_mfma_f32_16x16x32_f16 v[34:37], v[74:77], v[90:93], v[34:37]
	s_mov_b64 s[0:1], 0x780
	s_waitcnt vmcnt(4)
	s_barrier
	v_lshl_add_u64 v[70:71], v[4:5], 0, s[0:1]
	s_mov_b32 s4, m0
	s_mov_b32 m0, s17
	s_nop 0
	global_load_lds_dwordx4 v[70:71], off
	s_mov_b32 m0, s4
	v_lshl_add_u64 v[70:71], v[6:7], 0, s[0:1]
	s_mov_b32 s0, m0
	s_mov_b32 m0, s19
	s_nop 0
	global_load_lds_dwordx4 v[70:71], off
	s_mov_b32 m0, s0
	ds_read_b128 v[70:73], v2 offset:32768
	ds_read_b128 v[74:77], v2 offset:34816
	ds_read_b128 v[78:81], v10 offset:49152
	ds_read_b128 v[82:85], v10 offset:51200
	ds_read_b128 v[86:89], v10 offset:53248
	ds_read_b128 v[90:93], v10 offset:55296
	s_waitcnt lgkmcnt(9)
	v_mfma_f32_16x16x32_f16 v[58:61], v[42:45], v[50:53], v[58:61]
	s_waitcnt lgkmcnt(8)
	v_mfma_f32_16x16x32_f16 v[62:65], v[42:45], v[54:57], v[62:65]
	s_waitcnt lgkmcnt(7)
	v_mfma_f32_16x16x32_f16 v[66:69], v[42:45], v[94:97], v[66:69]
	s_waitcnt lgkmcnt(6)
	v_mfma_f32_16x16x32_f16 v[30:33], v[42:45], v[98:101], v[30:33]
	v_mfma_f32_16x16x32_f16 v[38:41], v[46:49], v[50:53], v[38:41]
	v_mfma_f32_16x16x32_f16 v[22:25], v[46:49], v[54:57], v[22:25]
	v_mfma_f32_16x16x32_f16 v[26:29], v[46:49], v[94:97], v[26:29]
	v_mfma_f32_16x16x32_f16 v[34:37], v[46:49], v[98:101], v[34:37]
	s_mov_b64 s[0:1], 0x22780
	v_lshl_add_u64 v[4:5], v[4:5], 0, s[0:1]
	s_mov_b32 s4, m0
	s_mov_b32 m0, s2
	s_nop 0
	global_load_lds_dwordx4 v[4:5], off
	s_mov_b32 m0, s4
	v_lshl_add_u64 v[4:5], v[6:7], 0, s[0:1]
	s_mov_b32 s0, m0
	s_mov_b32 m0, s3
	s_nop 0
	global_load_lds_dwordx4 v[4:5], off
	s_mov_b32 m0, s0
	ds_read_b128 v[4:7], v12 offset:32768
	ds_read_b128 v[42:45], v12 offset:34816
	ds_read_b128 v[46:49], v11 offset:49152
	ds_read_b128 v[50:53], v11 offset:51200
	ds_read_b128 v[54:57], v11 offset:53248
	ds_read_b128 v[94:97], v11 offset:55296
	s_waitcnt lgkmcnt(9)
	v_mfma_f32_16x16x32_f16 v[58:61], v[70:73], v[78:81], v[58:61]
	s_waitcnt lgkmcnt(8)
	v_mfma_f32_16x16x32_f16 v[62:65], v[70:73], v[82:85], v[62:65]
	s_waitcnt lgkmcnt(7)
	v_mfma_f32_16x16x32_f16 v[66:69], v[70:73], v[86:89], v[66:69]
	s_waitcnt lgkmcnt(6)
	v_mfma_f32_16x16x32_f16 v[30:33], v[70:73], v[90:93], v[30:33]
	v_mfma_f32_16x16x32_f16 v[38:41], v[74:77], v[78:81], v[38:41]
	v_mfma_f32_16x16x32_f16 v[22:25], v[74:77], v[82:85], v[22:25]
	v_mfma_f32_16x16x32_f16 v[26:29], v[74:77], v[86:89], v[26:29]
	v_mfma_f32_16x16x32_f16 v[34:37], v[74:77], v[90:93], v[34:37]
	s_waitcnt vmcnt(4)
	s_barrier
	ds_read_b128 v[70:73], v14
	ds_read_b128 v[74:77], v14 offset:2048
	ds_read_b128 v[78:81], v13 offset:6144
	ds_read_b128 v[82:85], v13 offset:4096
	ds_read_b128 v[86:89], v13 offset:2048
	ds_read_b128 v[10:13], v13
	s_waitcnt lgkmcnt(9)
	v_mfma_f32_16x16x32_f16 v[58:61], v[4:7], v[46:49], v[58:61]
	s_waitcnt lgkmcnt(8)
	v_mfma_f32_16x16x32_f16 v[62:65], v[4:7], v[50:53], v[62:65]
	s_waitcnt lgkmcnt(7)
	v_mfma_f32_16x16x32_f16 v[66:69], v[4:7], v[54:57], v[66:69]
	s_waitcnt lgkmcnt(6)
	v_mfma_f32_16x16x32_f16 v[4:7], v[4:7], v[94:97], v[30:33]
	v_mfma_f32_16x16x32_f16 v[30:33], v[42:45], v[46:49], v[38:41]
	v_mfma_f32_16x16x32_f16 v[22:25], v[42:45], v[50:53], v[22:25]
	v_mfma_f32_16x16x32_f16 v[26:29], v[42:45], v[54:57], v[26:29]
	v_mfma_f32_16x16x32_f16 v[34:37], v[42:45], v[94:97], v[34:37]
	ds_read_b128 v[38:41], v16
	ds_read_b128 v[42:45], v16 offset:2048
	ds_read_b128 v[46:49], v15
	ds_read_b128 v[50:53], v15 offset:2048
	ds_read_b128 v[54:57], v15 offset:4096
	ds_read_b128 v[90:93], v15 offset:6144
	s_waitcnt lgkmcnt(6)
	v_mfma_f32_16x16x32_f16 v[58:61], v[70:73], v[10:13], v[58:61]
	v_mfma_f32_16x16x32_f16 v[62:65], v[70:73], v[86:89], v[62:65]
	v_mfma_f32_16x16x32_f16 v[66:69], v[70:73], v[82:85], v[66:69]
	v_mfma_f32_16x16x32_f16 v[4:7], v[70:73], v[78:81], v[4:7]
	v_mfma_f32_16x16x32_f16 v[10:13], v[74:77], v[10:13], v[30:33]
	v_mfma_f32_16x16x32_f16 v[22:25], v[74:77], v[86:89], v[22:25]
	v_mfma_f32_16x16x32_f16 v[26:29], v[74:77], v[82:85], v[26:29]
	v_mfma_f32_16x16x32_f16 v[30:33], v[74:77], v[78:81], v[34:37]
	s_waitcnt vmcnt(0)
	s_barrier
	s_nop 1
	ds_read_b128 v[34:37], v18 offset:6144
	ds_read_b128 v[70:73], v18 offset:4096
	ds_read_b128 v[74:77], v18 offset:2048
	ds_read_b128 v[78:81], v18
	ds_read_b128 v[82:85], v17 offset:2048
	ds_read_b128 v[14:17], v17
	s_waitcnt lgkmcnt(9)
	v_mfma_f32_16x16x32_f16 v[58:61], v[38:41], v[46:49], v[58:61]
	s_waitcnt lgkmcnt(8)
	v_mfma_f32_16x16x32_f16 v[62:65], v[38:41], v[50:53], v[62:65]
	s_waitcnt lgkmcnt(7)
	v_mfma_f32_16x16x32_f16 v[66:69], v[38:41], v[54:57], v[66:69]
	s_waitcnt lgkmcnt(6)
	v_mfma_f32_16x16x32_f16 v[4:7], v[38:41], v[90:93], v[4:7]
	v_mfma_f32_16x16x32_f16 v[10:13], v[42:45], v[46:49], v[10:13]
	v_mfma_f32_16x16x32_f16 v[22:25], v[42:45], v[50:53], v[22:25]
	v_mfma_f32_16x16x32_f16 v[26:29], v[42:45], v[54:57], v[26:29]
	v_mfma_f32_16x16x32_f16 v[30:33], v[42:45], v[90:93], v[30:33]
	ds_read_b128 v[38:41], v20
	ds_read_b128 v[42:45], v20 offset:2048
	ds_read_b128 v[46:49], v20 offset:4096
	ds_read_b128 v[50:53], v20 offset:6144
	ds_read_b128 v[54:57], v19 offset:2048
	ds_read_b128 v[18:21], v19
	v_and_b32_e32 v0, 64, v0
	s_waitcnt lgkmcnt(6)
	v_mfma_f32_16x16x32_f16 v[58:61], v[14:17], v[78:81], v[58:61]
	v_mfma_f32_16x16x32_f16 v[62:65], v[14:17], v[74:77], v[62:65]
	v_mfma_f32_16x16x32_f16 v[66:69], v[14:17], v[70:73], v[66:69]
	v_mfma_f32_16x16x32_f16 v[4:7], v[14:17], v[34:37], v[4:7]
	v_mfma_f32_16x16x32_f16 v[10:13], v[82:85], v[78:81], v[10:13]
	v_mfma_f32_16x16x32_f16 v[14:17], v[82:85], v[74:77], v[22:25]
	v_mfma_f32_16x16x32_f16 v[22:25], v[82:85], v[70:73], v[26:29]
	v_mfma_f32_16x16x32_f16 v[26:29], v[82:85], v[34:37], v[30:33]
	s_waitcnt lgkmcnt(0)
	v_mfma_f32_16x16x32_f16 v[30:33], v[18:21], v[38:41], v[58:61]
	v_mfma_f32_16x16x32_f16 v[34:37], v[18:21], v[42:45], v[62:65]
	v_mfma_f32_16x16x32_f16 v[58:61], v[18:21], v[46:49], v[66:69]
	v_mfma_f32_16x16x32_f16 v[4:7], v[18:21], v[50:53], v[4:7]
	v_mfma_f32_16x16x32_f16 v[10:13], v[54:57], v[38:41], v[10:13]
	v_mfma_f32_16x16x32_f16 v[14:17], v[54:57], v[42:45], v[14:17]
	v_mfma_f32_16x16x32_f16 v[18:21], v[54:57], v[46:49], v[22:25]
	v_mfma_f32_16x16x32_f16 v[22:25], v[54:57], v[50:53], v[26:29]
	s_lshl_b32 s0, s13, 7
	v_or3_b32 v0, s0, v0, v9
	v_lshlrev_b32_e32 v2, 2, v0
	global_load_dword v46, v2, s[8:9]
	global_load_dword v47, v2, s[8:9] offset:64
	global_load_dword v48, v2, s[8:9] offset:128
	global_load_dword v49, v2, s[8:9] offset:192
	v_and_b32_e32 v0, 12, v1
	v_or3_b32 v0, s12, v8, v0
	v_ashrrev_i32_e32 v1, 31, v0
	v_or_b32_e32 v8, 1, v0
	v_or_b32_e32 v26, 2, v0
	v_or_b32_e32 v28, 3, v0
	v_or_b32_e32 v38, 16, v0
	v_or_b32_e32 v40, 17, v0
	v_or_b32_e32 v42, 18, v0
	v_or_b32_e32 v44, 19, v0
	v_lshl_add_u64 v[2:3], s[10:11], 0, v[2:3]
	v_lshlrev_b64 v[0:1], 12, v[0:1]
	v_ashrrev_i32_e32 v9, 31, v8
	v_ashrrev_i32_e32 v27, 31, v26
	v_ashrrev_i32_e32 v29, 31, v28
	v_ashrrev_i32_e32 v39, 31, v38
	v_ashrrev_i32_e32 v41, 31, v40
	v_ashrrev_i32_e32 v43, 31, v42
	v_ashrrev_i32_e32 v45, 31, v44
	v_lshl_add_u64 v[0:1], v[2:3], 0, v[0:1]
	v_lshlrev_b64 v[8:9], 12, v[8:9]
	v_lshlrev_b64 v[26:27], 12, v[26:27]
	v_lshlrev_b64 v[28:29], 12, v[28:29]
	v_lshlrev_b64 v[38:39], 12, v[38:39]
	v_lshlrev_b64 v[40:41], 12, v[40:41]
	v_lshlrev_b64 v[42:43], 12, v[42:43]
	v_lshlrev_b64 v[44:45], 12, v[44:45]
	v_lshl_add_u64 v[8:9], v[2:3], 0, v[8:9]
	v_lshl_add_u64 v[26:27], v[2:3], 0, v[26:27]
	v_lshl_add_u64 v[28:29], v[2:3], 0, v[28:29]
	v_lshl_add_u64 v[38:39], v[2:3], 0, v[38:39]
	v_lshl_add_u64 v[40:41], v[2:3], 0, v[40:41]
	v_lshl_add_u64 v[42:43], v[2:3], 0, v[42:43]
	v_lshl_add_u64 v[2:3], v[2:3], 0, v[44:45]
	s_waitcnt vmcnt(3)
	v_add_f32_e32 v30, v46, v30
	v_add_f32_e32 v31, v46, v31
	v_add_f32_e32 v32, v46, v32
	s_waitcnt vmcnt(0)
	v_add_f32_e32 v4, v49, v4
	v_add_f32_e32 v33, v46, v33
	v_add_f32_e32 v10, v46, v10
	v_add_f32_e32 v11, v46, v11
	v_add_f32_e32 v12, v46, v12
	v_add_f32_e32 v13, v46, v13
	v_add_f32_e32 v34, v47, v34
	v_add_f32_e32 v35, v47, v35
	v_add_f32_e32 v36, v47, v36
	v_add_f32_e32 v37, v47, v37
	v_add_f32_e32 v14, v47, v14
	v_add_f32_e32 v15, v47, v15
	v_add_f32_e32 v16, v47, v16
	v_add_f32_e32 v17, v47, v17
	v_add_f32_e32 v44, v48, v58
	v_add_f32_e32 v45, v48, v59
	v_add_f32_e32 v46, v48, v60
	v_add_f32_e32 v47, v48, v61
	v_add_f32_e32 v18, v48, v18
	v_add_f32_e32 v19, v48, v19
	global_store_dword v[0:1], v30, off sc0 sc1 nt
	global_store_dword v[8:9], v31, off sc0 sc1 nt
	global_store_dword v[26:27], v32, off sc0 sc1 nt
	global_store_dword v[28:29], v33, off sc0 sc1 nt
	global_store_dword v[38:39], v10, off sc0 sc1 nt
	global_store_dword v[40:41], v11, off sc0 sc1 nt
	global_store_dword v[42:43], v12, off sc0 sc1 nt
	global_store_dword v[2:3], v13, off sc0 sc1 nt
	global_store_dword v[0:1], v34, off offset:64 sc0 sc1 nt
	global_store_dword v[8:9], v35, off offset:64 sc0 sc1 nt
	global_store_dword v[26:27], v36, off offset:64 sc0 sc1 nt
	global_store_dword v[28:29], v37, off offset:64 sc0 sc1 nt
	global_store_dword v[38:39], v14, off offset:64 sc0 sc1 nt
	global_store_dword v[40:41], v15, off offset:64 sc0 sc1 nt
	global_store_dword v[42:43], v16, off offset:64 sc0 sc1 nt
	global_store_dword v[2:3], v17, off offset:64 sc0 sc1 nt
	global_store_dword v[0:1], v44, off offset:128 sc0 sc1 nt
	global_store_dword v[8:9], v45, off offset:128 sc0 sc1 nt
	global_store_dword v[26:27], v46, off offset:128 sc0 sc1 nt
	global_store_dword v[28:29], v47, off offset:128 sc0 sc1 nt
	global_store_dword v[38:39], v18, off offset:128 sc0 sc1 nt
	global_store_dword v[40:41], v19, off offset:128 sc0 sc1 nt
	global_store_dword v[0:1], v4, off offset:192 sc0 sc1 nt
	v_add_f32_e32 v0, v49, v5
	global_store_dword v[8:9], v0, off offset:192 sc0 sc1 nt
	v_add_f32_e32 v0, v49, v6
	global_store_dword v[26:27], v0, off offset:192 sc0 sc1 nt
	v_add_f32_e32 v0, v49, v7
	global_store_dword v[28:29], v0, off offset:192 sc0 sc1 nt
	v_add_f32_e32 v0, v49, v22
	global_store_dword v[38:39], v0, off offset:192 sc0 sc1 nt
	v_add_f32_e32 v0, v49, v23
	v_add_f32_e32 v10, v48, v20
	global_store_dword v[40:41], v0, off offset:192 sc0 sc1 nt
	v_add_f32_e32 v0, v49, v24
	global_store_dword v[42:43], v10, off offset:128 sc0 sc1 nt
	v_add_f32_e32 v10, v48, v21
	global_store_dword v[42:43], v0, off offset:192 sc0 sc1 nt
	v_add_f32_e32 v0, v49, v25
	global_store_dword v[2:3], v10, off offset:128 sc0 sc1 nt
	global_store_dword v[2:3], v0, off offset:192 sc0 sc1 nt
	s_endpgm
